# P7 K-tile LDS swizzle g(row)=(row&3)|((row>>3)&3)<<2 (conflict-free ds_read_b128 lane groups), padded to keep the later code at the previous placement mod 64
# baseline (speedup 1.0000x reference)
.Lp7prio:
	v_lshrrev_b32_e32 v1, 4, v0
	v_lshrrev_b32_e32 v9, 3, v0
	v_and_b32_e32 v9, 8, v9
	v_or_b32_e32 v15, 32, v1
	v_lshlrev_b32_e32 v5, 3, v0
	v_and_or_b32 v10, v1, 16, v9
	v_and_or_b32 v9, v15, 48, v9
	v_and_b32_e32 v7, 0x78, v5
	v_lshrrev_b32_e32 v11, 5, v0
	v_lshrrev_b32_e32 v10, 1, v10
	v_bfe_u32 v12, v5, 5, 2
	v_bfe_u32 v13, v0, 4, 2
	v_lshrrev_b32_e32 v9, 1, v9
	v_or_b32_e32 v10, v10, v12
	v_and_or_b32 v11, v11, 4, v13
	v_lshlrev_b32_e32 v13, 1, v7
	v_or_b32_e32 v9, v9, v12
	v_lshlrev_b32_e32 v10, 9, v10
	v_lshlrev_b32_e32 v11, 6, v11
	v_and_b32_e32 v14, 48, v13
	v_lshlrev_b32_e32 v9, 9, v9
	v_or3_b32 v10, v10, v11, v14
	v_or3_b32 v9, v9, v11, v14
	v_lshlrev_b32_e32 v11, 4, v0
	v_lshlrev_b32_e32 v14, 1, v0
	v_and_b32_e32 v12, 0xc0, v11
	v_and_b32_e32 v14, 32, v14
	v_and_b32_e32 v5, 0x118, v5
	v_or3_b32 v12, v14, v12, v5
	v_mul_u32_u24_e32 v14, 0x2700, v1
	v_or_b32_e32 v5, v14, v7
	v_bfe_u32 v6, v0, 5, 1
	s_waitcnt vmcnt(23)
	v_lshlrev_b32_e32 v150, 1, v5
	v_lshlrev_b32_e32 v1, 8, v1
	v_lshrrev_b32_e32 v5, 1, v0
	v_and_b32_e32 v5, 0xc0, v5
	v_and_or_b32 v5, v0, 48, v5
	s_nop 0
	s_nop 0
	s_nop 0
	s_nop 0
	s_nop 0
	s_nop 0
	s_nop 0
	s_nop 0
	s_nop 0
	s_nop 0
	s_nop 0
	s_movk_i32 s4, 0x70
	v_bitop3_b32 v16, v13, v1, v5 bitop3:0xde
	v_lshlrev_b32_e32 v1, 8, v15
	v_lshlrev_b32_e32 v15, 4, v6
	v_bitop3_b32 v13, v13, v1, v5 bitop3:0xde
	v_lshlrev_b32_e32 v1, 3, v0
	v_and_b32_e32 v1, 0xc0, v1
	v_and_or_b32 v1, v11, 48, v1
	v_xor_b32_e32 v11, v15, v1
	s_movk_i32 s4, 0x60
	s_waitcnt vmcnt(0)
	v_bitop3_b32 v19, v15, v1, s4 bitop3:0x36
	s_movk_i32 s4, 0x80
	s_add_u32 s10, s44, 0x49098000
	v_and_b32_e32 v146, 31, v2
	v_mov_b32_e32 v149, 0
	v_and_b32_e32 v3, 63, v0
	s_movk_i32 s3, 0xc0
	v_bitop3_b32 v20, v15, v1, s4 bitop3:0x36
	s_movk_i32 s4, 0xa0
	v_lshrrev_b32_e32 v2, 1, v2
	s_addc_u32 s11, s45, 0
	v_and_b32_e32 v4, 31, v0
	v_bitop3_b32 v21, v15, v1, s4 bitop3:0x36
	v_bitop3_b32 v22, v15, v1, s3 bitop3:0x36
	s_movk_i32 s3, 0xe0
	v_cmp_gt_u32_e64 s[4:5], 32, v3
	v_mov_b32_e32 v5, v149
	v_and_b32_e32 v2, 16, v2
	v_mov_b32_e32 v3, v149
	v_and_b32_e32 v8, 0x1c0, v0
	v_bitop3_b32 v17, v15, v1, 32 bitop3:0x36
	v_bitop3_b32 v18, v15, v1, 64 bitop3:0x36
	v_bitop3_b32 v23, v15, v1, s3 bitop3:0x36
	v_lshlrev_b32_e32 v1, 2, v6
	v_lshlrev_b32_e32 v6, 12, v6
	v_mov_b32_e32 v7, v149
	v_lshl_add_u64 v[154:155], s[10:11], 0, v[2:3]
	s_add_i32 s6, 0, 0x10000
	v_lshl_add_u64 v[2:3], s[44:45], 0, v[4:5]
	v_lshl_add_u32 v8, v8, 2, s6
	v_lshl_add_u64 v[2:3], v[2:3], 0, v[6:7]
	s_mov_b64 s[6:7], 0x9aa98000
	v_lshlrev_b32_e32 v148, 10, v4
	v_lshl_add_u64 v[156:157], v[2:3], 0, s[6:7]
	s_add_i32 s6, 0, 0x4000
	v_add_u32_e32 v197, s6, v12
	v_lshl_add_u64 v[2:3], s[44:45], 0, v[148:149]
	s_mov_b64 s[6:7], 0x98a98000
	s_lshl_b32 s3, s52, 5
	v_lshl_add_u32 v5, v4, 8, 0
	v_lshl_add_u64 v[158:159], v[2:3], 0, s[6:7]
	v_and_b32_e32 v2, 15, v0
	v_lshlrev_b32_e32 v3, 1, v14
	v_add_u32_e32 v152, 0x9c000, v150
	v_mov_b32_e32 v151, v149
	v_mov_b32_e32 v153, v149
	s_and_b32 s3, s3, 32
	s_and_b32 s19, s66, 0xffffff80
	s_mov_b32 s13, 0
	v_add_u32_e32 v147, 0, v12
	v_lshl_add_u32 v196, v4, 2, v8
	s_movk_i32 s30, 0x4000
	v_add_u32_e32 v198, v8, v15
	v_lshl_or_b32 v160, v2, 4, v3
	v_mov_b32_e32 v161, v149
	s_mov_b64 s[14:15], 0xa00
	s_mov_b64 s[16:17], 0x800
	s_movk_i32 s31, 0x4e00
	s_mov_b32 s34, 0xff800000
	s_mov_b32 s35, 0x42b504f3
	s_mov_b32 s18, 0x3e0293ee
	s_mov_b32 s36, 0x49308000
	s_mov_b32 s37, 0x493a4000
	s_mov_b32 s38, 0x49440000
	s_mov_b32 s39, 0x494dc000
	s_mov_b64 s[20:21], 0x270000
	s_mov_b32 s40, 0xc3e00000
	s_movk_i32 s41, 0x2000
	s_movk_i32 s42, 0x6000
	v_mov_b32_e32 v149, 0x4e00
	v_add_u32_e32 v199, 0, v10
	v_add_u32_e32 v200, 0, v9
	v_add_u32_e32 v201, 0, v16
	v_add_u32_e32 v202, 0, v13
	v_add_u32_e32 v203, v5, v11
	v_add_u32_e32 v204, v5, v17
	v_add_u32_e32 v205, v5, v18
	v_add_u32_e32 v206, v5, v19
	v_add_u32_e32 v207, v5, v20
	v_add_u32_e32 v208, v5, v21
	v_add_u32_e32 v209, v5, v22
	v_add_u32_e32 v210, v5, v23
	v_mov_b32_e32 v211, 0xf149f2ca
	v_mov_b32_e32 v212, 0x43e00000
	s_mov_b32 s43, s2
	s_branch .LBB0_1719
